# row phases with gate/router weights: weight-fill loads land in unused registers, their wait and LDS writes deferred into the first block's prologue behind its own loads (counted vmcnt)
# baseline (speedup 1.0000x reference)
; template <int YMODE, int EXTRA, bool NORM_OUT, bool XN8  , bool XIN_BF = false  , bool XOUT_BF = false  > ...
;     ...
;     if (EXTRA) {
;         for (int k = F.tid; k < D; k += NTHR) { const f32x4 a = *(const f32x4*)(wex + (size_t)k * ldw), b = *(const f32x4*)(wex + (size_t)k * ldw + 4);
;             we[0 * D + k] = a[0]; we[1 * D + k] = a[1]; we[2 * D + k] = a[2]; we[3 * D + k] = a[3]; we[4 * D + k] = b[0]; we[5 * D + k] = b[1]; we[6 * D + k] = b[2]; we[7 * D + k] = b[3]; }
;     }
.LBB0_101:
	v_lshl_add_u64 v[16:17], v[2:3], 0, s[12:13]
	v_lshl_add_u64 v[18:19], v[16:17], 0, s[12:13]
	v_lshl_add_u64 v[20:21], v[18:19], 0, s[12:13]
	global_load_dwordx4 v[120:123], v[2:3], off offset:-16
	global_load_dwordx4 v[124:127], v[2:3], off
	global_load_dwordx4 v[128:131], v[16:17], off offset:-16
	global_load_dwordx4 v[132:135], v[16:17], off
	global_load_dwordx4 v[136:139], v[18:19], off offset:-16
	global_load_dwordx4 v[140:143], v[18:19], off
	global_load_dwordx4 v[144:147], v[20:21], off offset:-16
	global_load_dwordx4 v[148:151], v[20:21], off
	v_mov_b32_e32 v152, v5
	s_cmpk_gt_i32 s2, 0xff
	s_cbranch_scc1 .LBB0_120
	v_lshlrev_b32_e32 v66, 2, v1
	v_mov_b32_e32 v67, 0
	v_lshl_add_u64 v[68:69], s[8:9], 0, v[66:67]
	v_lshl_add_u64 v[2:3], s[50:51], 0, v[66:67]
	s_mov_b64 s[8:9], 0x102000
	s_add_u32 s3, s50, 0x400000
	v_lshl_add_u64 v[70:71], v[2:3], 0, s[8:9]
	s_mov_b64 s[8:9], 0x100000
	s_addc_u32 s4, s51, 0
	s_add_i32 s10, 0, 0x12000
	v_lshl_add_u64 v[72:73], v[2:3], 0, s[8:9]
	s_add_i32 s8, 0, 0x14000
	v_add_u32_e32 v84, s10, v66
	v_add_u32_e32 v85, s8, v66
	v_lshlrev_b32_e32 v66, 2, v194
	v_lshlrev_b32_e32 v2, 4, v194
	v_mov_b32_e32 v3, v67
	v_lshl_add_u64 v[4:5], s[28:29], 0, v[66:67]
	v_lshl_add_u64 v[74:75], s[6:7], 0, v[2:3]
	v_add_u32_e32 v86, s10, v2
	v_add_u32_e32 v87, s8, v2
	v_add_u32_e32 v88, 0, v2
	v_lshl_add_u64 v[2:3], s[26:27], 0, v[66:67]
	v_lshl_add_u64 v[4:5], v[4:5], 0, -16
	v_cmp_gt_u32_e32 vcc, 4, v194
	s_mov_b64 s[26:27], 0x200000
	v_readlane_b32 s5, v255, 9
	v_cndmask_b32_e32 v77, v5, v3, vcc
	v_cndmask_b32_e32 v76, v4, v2, vcc
	v_lshl_add_u64 v[2:3], s[50:51], 0, v[66:67]
	v_lshl_add_u64 v[78:79], v[2:3], 0, s[26:27]
	s_mov_b64 s[26:27], 0x18a00000
	s_lshl_b32 s5, s5, 3
	v_cmp_eq_u32_e64 s[6:7], 0, v194
	v_cmp_gt_u32_e64 s[8:9], 8, v194
	v_cmp_eq_u32_e64 s[10:11], 7, v194
	v_cmp_eq_u32_e64 s[12:13], 6, v194
	v_cmp_eq_u32_e64 s[14:15], 5, v194
	v_cmp_eq_u32_e64 s[16:17], 4, v194
	v_cmp_eq_u32_e64 s[18:19], 3, v194
	v_cmp_eq_u32_e64 s[20:21], 2, v194
	v_cmp_eq_u32_e64 s[22:23], 1, v194
	v_cmp_lt_u32_e64 s[24:25], 3, v194
	v_lshl_add_u64 v[80:81], v[2:3], 0, s[26:27]
	v_mov_b32_e32 v66, 0x358637bd
	s_mov_b32 s33, 0xf800000
	v_mov_b32_e32 v89, 0x260
	s_mov_b32 s40, 0x42fe0000
	s_mov_b32 s41, 0xc2fe0000
	s_mov_b32 s42, 0x40c0c00
	s_mov_b32 s43, 0x3f200000
	s_mov_b32 s44, 0x3fb8aa3b
	s_mov_b32 s45, 0xc2ce8ed0
	s_mov_b32 s46, 0x42b17218
	s_mov_b32 s47, 0x7f800000
	v_mov_b32_e32 v90, 0x3ca908c9
	s_brev_b32 s49, -2
	s_mov_b32 s52, 0xbfb8aa3b
	s_mov_b32 s53, 0xb2a5705f
	s_mov_b32 s54, 0x42ce8ed0
	s_mov_b32 s55, 0xc2b17218
	s_mov_b32 s56, 0x3f2aaaab
	v_mov_b32_e32 v91, 0x3ecc95a3
	s_mov_b32 s57, 0x3f317218
	s_mov_b32 s58, 0x33800000
	v_mov_b32_e32 v92, 0x3a000000
	v_mov_b32_e32 v93, 0x42fe0000
	v_mov_b32_e32 v94, 0x7f800000
	v_mov_b32_e32 v82, 0x3f317218
	s_mov_b32 s28, s2
	s_branch .LBB0_105

; #define LAS __attribute__((address_space(3)))
; template <int YMODE, int EXTRA, bool NORM_OUT, bool XN8  , bool XIN_BF = false  , bool XOUT_BF = false  > ...
;     ...
;         for (int k = F.tid; k < D; k += NTHR) { const f32x4 a = *(const f32x4*)(wex + (size_t)k * ldw), b = *(const f32x4*)(wex + (size_t)k * ldw + 4);
;             we[0 * D + k] = a[0]; we[1 * D + k] = a[1]; we[2 * D + k] = a[2]; we[3 * D + k] = a[3]; we[4 * D + k] = b[0]; we[5 * D + k] = b[1]; we[6 * D + k] = b[2]; we[7 * D + k] = b[3]; }
;     ...
;     for (int blk = blockIdx.x; blk < M / 64; blk += F.G) {
;         const int b = (blk * 64) / SEQ;
;         __syncthreads();
;         { const int col = 4 * F.tid;
;             if (YMODE) { const f32x4 g = *(const f32x4*)(gt + (size_t)b * 6 * D + col), p = *(const f32x4*)(gpost + col); *(LAS f32x4*)(vA + col) = g * p; }
;             if (NORM_OUT) { const f32x4 g = *(const f32x4*)(gpre + col), s = *(const f32x4*)(sc + (size_t)b * 6 * D + col); *(LAS f32x4*)(vB + col) = g * (1.f + s); *(LAS f32x4*)(vC + col) = *(const f32x4*)(sh + (size_t)b * 6 * D + col); } }
;         __syncthreads();
;         f32x4 xr[8]; u32x2 xrb[8], yr[8], yr2[8]; float w1n = 0.f, w2n = 0.f;
;     ...
;         RP_LOAD(0);
.LBB0_105:
	s_ashr_i32 s29, s28, 31
	s_lshr_b32 s26, s29, 27
	s_add_i32 s26, s28, s26
	s_ashr_i32 s26, s26, 5
	s_mul_i32 s26, s26, 6
	s_ashr_i32 s27, s26, 31
	s_lshl_b64 s[26:27], s[26:27], 13
	v_lshl_add_u64 v[2:3], v[70:71], 0, s[26:27]
	s_waitcnt lgkmcnt(0)
	s_barrier
	global_load_dwordx4 v[2:5], v[2:3], off
	v_lshl_add_u64 v[6:7], v[72:73], 0, s[26:27]
	global_load_dwordx4 v[6:9], v[6:7], off
	s_nop 0
	global_load_dwordx4 v[10:13], v[68:69], off
	s_lshl_b64 s[30:31], s[28:29], 6
	s_add_u32 s29, s30, s5
	s_addc_u32 s35, s31, 0
	s_and_b32 s26, s28, 7
	s_or_b32 s34, s29, s26
	s_lshl_b64 s[26:27], s[34:35], 13
	v_lshl_add_u64 v[14:15], v[74:75], 0, s[26:27]
	v_add_co_u32_e32 v16, vcc, 0x1000, v14
	s_mov_b32 s59, 0
	s_nop 0
	v_addc_co_u32_e32 v17, vcc, 0, v15, vcc
	global_load_dwordx4 v[62:65], v[14:15], off nt
	global_load_dwordx4 v[58:61], v[14:15], off offset:1024 nt
	global_load_dwordx4 v[54:57], v[14:15], off offset:2048 nt
	global_load_dwordx4 v[50:53], v[14:15], off offset:3072 nt
	global_load_dwordx4 v[46:49], v[16:17], off nt
	global_load_dwordx4 v[42:45], v[16:17], off offset:1024 nt
	global_load_dwordx4 v[38:41], v[16:17], off offset:2048 nt
	global_load_dwordx4 v[34:37], v[16:17], off offset:3072 nt
	s_waitcnt vmcnt(11)
	ds_write2st64_b32 v152, v120, v121 offset0:0 offset1:32
	ds_write2st64_b32 v152, v122, v123 offset0:64 offset1:96
	ds_write2st64_b32 v152, v124, v125 offset0:128 offset1:160
	ds_write2st64_b32 v152, v126, v127 offset0:192 offset1:224
	ds_write2st64_b32 v152, v128, v129 offset0:8 offset1:40
	ds_write2st64_b32 v152, v130, v131 offset0:72 offset1:104
	ds_write2st64_b32 v152, v132, v133 offset0:136 offset1:168
	ds_write2st64_b32 v152, v134, v135 offset0:200 offset1:232
	ds_write2st64_b32 v152, v136, v137 offset0:16 offset1:48
	ds_write2st64_b32 v152, v138, v139 offset0:80 offset1:112
	ds_write2st64_b32 v152, v140, v141 offset0:144 offset1:176
	ds_write2st64_b32 v152, v142, v143 offset0:208 offset1:240
	ds_write2st64_b32 v152, v144, v145 offset0:24 offset1:56
	ds_write2st64_b32 v152, v146, v147 offset0:88 offset1:120
	ds_write2st64_b32 v152, v148, v149 offset0:152 offset1:184
	ds_write2st64_b32 v152, v150, v151 offset0:216 offset1:248
	s_waitcnt vmcnt(8)
	v_pk_add_f32 v[4:5], v[4:5], 1.0 op_sel_hi:[1,0]
	v_pk_add_f32 v[2:3], v[2:3], 1.0 op_sel_hi:[1,0]
	s_waitcnt lgkmcnt(0)
	v_pk_mul_f32 v[4:5], v[12:13], v[4:5]
	v_pk_mul_f32 v[2:3], v[10:11], v[2:3]
	ds_write_b128 v85, v[6:9]
	ds_write_b128 v84, v[2:5]
	s_waitcnt lgkmcnt(0)
	s_barrier
	s_waitcnt vmcnt(0) lgkmcnt(0)
	v_mov_b64_e32 v[2:3], v[62:63]
	v_mov_b64_e32 v[6:7], v[58:59]
	v_mov_b64_e32 v[10:11], v[54:55]
	v_mov_b64_e32 v[14:15], v[50:51]
	v_mov_b64_e32 v[18:19], v[46:47]
	v_mov_b64_e32 v[22:23], v[42:43]
	v_mov_b64_e32 v[26:27], v[38:39]
	v_mov_b64_e32 v[30:31], v[34:35]
	v_mov_b64_e32 v[4:5], v[64:65]
	v_mov_b64_e32 v[8:9], v[60:61]
	v_mov_b64_e32 v[12:13], v[56:57]
	v_mov_b64_e32 v[16:17], v[52:53]
	v_mov_b64_e32 v[20:21], v[48:49]
	v_mov_b64_e32 v[24:25], v[44:45]
	v_mov_b64_e32 v[28:29], v[40:41]
	v_mov_b64_e32 v[32:33], v[36:37]
	s_branch .LBB0_108

; template <int YMODE, int EXTRA, bool NORM_OUT, bool XN8  , bool XIN_BF = false  , bool XOUT_BF = false  > ...
;     ...
;     if (EXTRA) {
;         for (int k = F.tid; k < D; k += NTHR) { const f32x4 a = *(const f32x4*)(wex + (size_t)k * ldw), b = *(const f32x4*)(wex + (size_t)k * ldw + 4);
;             we[0 * D + k] = a[0]; we[1 * D + k] = a[1]; we[2 * D + k] = a[2]; we[3 * D + k] = a[3]; we[4 * D + k] = b[0]; we[5 * D + k] = b[1]; we[6 * D + k] = b[2]; we[7 * D + k] = b[3]; }
;     }
.LBB0_1300:
	v_lshl_add_u64 v[16:17], v[2:3], 0, s[10:11]
	v_lshl_add_u64 v[18:19], v[16:17], 0, s[10:11]
	v_lshl_add_u64 v[20:21], v[18:19], 0, s[10:11]
	global_load_dwordx4 v[146:149], v[2:3], off offset:-16
	global_load_dwordx4 v[150:153], v[2:3], off
	global_load_dwordx4 v[154:157], v[16:17], off offset:-16
	global_load_dwordx4 v[158:161], v[16:17], off
	global_load_dwordx4 v[162:165], v[18:19], off offset:-16
	global_load_dwordx4 v[166:169], v[18:19], off
	global_load_dwordx4 v[170:173], v[20:21], off offset:-16
	global_load_dwordx4 v[174:177], v[20:21], off
	v_mov_b32_e32 v178, v5
	s_cmpk_gt_i32 s2, 0xff
	s_cbranch_scc1 .LBB0_1318
	s_add_u32 s3, s50, 0x400000
	v_lshlrev_b32_e32 v2, 2, v1
	v_mov_b32_e32 v3, 0
	s_addc_u32 s4, s51, 0
	v_lshl_add_u64 v[8:9], s[0:1], 0, v[2:3]
	s_mov_b64 s[0:1], 0x2000
	s_add_u32 s30, s12, 16
	v_lshl_add_u64 v[12:13], s[50:51], 0, v[2:3]
	v_lshl_add_u64 v[8:9], v[8:9], 0, s[0:1]
	s_mov_b64 s[0:1], 0x162000
	s_addc_u32 s31, s13, 0
	s_mov_b64 s[8:9], 0x10a000
	v_lshl_add_u64 v[6:7], s[6:7], 0, v[2:3]
	s_add_i32 s6, 0, 0x10000
	v_lshl_add_u64 v[10:11], v[12:13], 0, s[0:1]
	s_mov_b64 s[0:1], 0x160000
	v_lshl_add_u64 v[4:5], v[12:13], 0, s[8:9]
	v_add_u32_e32 v100, s6, v2
	s_add_i32 s6, 0, 0x12000
	v_lshl_add_u64 v[12:13], v[12:13], 0, s[0:1]
	s_add_i32 s7, 0, 0x14000
	v_readlane_b32 s0, v255, 9
	v_lshlrev_b32_e32 v16, 3, v194
	v_mov_b32_e32 v17, v3
	v_lshlrev_b32_e32 v1, 4, v194
	s_lshl_b32 s40, s0, 3
	v_lshl_add_u64 v[14:15], s[50:51], 0, v[16:17]
	s_mov_b64 s[0:1], 0x32a00000
	v_add_u32_e32 v103, s6, v1
	v_add_u32_e32 v104, s7, v1
	v_add_u32_e32 v105, 0, v1
	v_mov_b32_e32 v1, s27
	v_mov_b32_e32 v18, s31
	v_cmp_gt_u32_e32 vcc, 4, v194
	v_lshl_add_u64 v[14:15], v[14:15], 0, s[0:1]
	v_readlane_b32 s0, v255, 15
	v_cndmask_b32_e32 v19, v1, v18, vcc
	v_mov_b32_e32 v1, s26
	v_mov_b32_e32 v18, s30
	v_add_u32_e32 v101, s6, v2
	v_add_u32_e32 v102, s7, v2
	v_lshlrev_b32_e32 v2, 2, v194
	v_cndmask_b32_e32 v18, v1, v18, vcc
	v_readlane_b32 s1, v255, 16
	v_lshl_add_u64 v[16:17], s[72:73], 0, v[16:17]
	v_cmp_eq_u32_e64 s[6:7], 0, v194
	v_cmp_gt_u32_e64 s[8:9], 8, v194
	v_cmp_eq_u32_e64 s[10:11], 7, v194
	v_cmp_eq_u32_e64 s[12:13], 6, v194
	v_cmp_eq_u32_e64 s[14:15], 5, v194
	v_cmp_eq_u32_e64 s[16:17], 4, v194
	v_cmp_eq_u32_e64 s[18:19], 3, v194
	v_cmp_eq_u32_e64 s[20:21], 2, v194
	v_cmp_eq_u32_e64 s[22:23], 1, v194
	v_cmp_lt_u32_e64 s[24:25], 3, v194
	v_lshl_add_u64 v[18:19], v[18:19], 0, v[2:3]
	v_lshl_add_u64 v[20:21], s[0:1], 0, v[2:3]
	v_lshl_add_u64 v[22:23], s[60:61], 0, v[2:3]
	v_mov_b32_e32 v2, 0x358637bd
	s_mov_b32 s41, 0xf800000
	v_mov_b32_e32 v106, 0x260
	s_mov_b32 s42, 0xc2fe0000
	s_mov_b32 s43, 0x40c0c00
	s_mov_b32 s44, 0x42b17218
	s_mov_b32 s45, 0x7f800000
	v_mov_b32_e32 v107, 0x3ca908c9
	s_brev_b32 s46, -2
	s_mov_b32 s47, 0xbfb8aa3b
	s_mov_b32 s49, 0xb2a5705f
	s_mov_b32 s52, 0x42ce8ed0
	s_mov_b32 s53, 0xc2b17218
	s_mov_b32 s54, 0x3f2aaaab
	v_mov_b32_e32 v108, 0x3ecc95a3
	s_mov_b32 s55, 0x3f317218
	s_mov_b32 s56, 0x33800000
	v_mov_b32_e32 v109, 0x3a000000
	v_mov_b32_e32 v110, 0x42fe0000
	v_mov_b32_e32 v111, 0x7f800000
	v_mov_b32_e32 v24, 0x3f317218
	s_mov_b32 s0, s2
	s_branch .LBB0_1304

; #define LAS __attribute__((address_space(3)))
; template <int YMODE, int EXTRA, bool NORM_OUT, bool XN8  , bool XIN_BF = false  , bool XOUT_BF = false  > ...
;     ...
;         for (int k = F.tid; k < D; k += NTHR) { const f32x4 a = *(const f32x4*)(wex + (size_t)k * ldw), b = *(const f32x4*)(wex + (size_t)k * ldw + 4);
;             we[0 * D + k] = a[0]; we[1 * D + k] = a[1]; we[2 * D + k] = a[2]; we[3 * D + k] = a[3]; we[4 * D + k] = b[0]; we[5 * D + k] = b[1]; we[6 * D + k] = b[2]; we[7 * D + k] = b[3]; }
;     }
;     if (YMODE == 2) { if (F.tid == 0) { int cum = 0; for (int e = 0; e < NE; ++e) { cumt[e] = cum; cum += (int)((__hip_atomic_load(cntw + e, __ATOMIC_RELAXED, __HIP_MEMORY_SCOPE_AGENT) + 255u) >> 8); } } }
;     for (int blk = blockIdx.x; blk < M / 64; blk += F.G) {
;         const int b = (blk * 64) / SEQ;
;         __syncthreads();
;         { const int col = 4 * F.tid;
;             if (YMODE) { const f32x4 g = *(const f32x4*)(gt + (size_t)b * 6 * D + col), p = *(const f32x4*)(gpost + col); *(LAS f32x4*)(vA + col) = g * p; }
;             if (NORM_OUT) { const f32x4 g = *(const f32x4*)(gpre + col), s = *(const f32x4*)(sc + (size_t)b * 6 * D + col); *(LAS f32x4*)(vB + col) = g * (1.f + s); *(LAS f32x4*)(vC + col) = *(const f32x4*)(sh + (size_t)b * 6 * D + col); } }
;         __syncthreads();
;         f32x4 xr[8]; u32x2 xrb[8], yr[8], yr2[8]; float w1n = 0.f, w2n = 0.f;
;     ...
;         RP_LOAD(0);
.LBB0_1304:
	s_ashr_i32 s1, s0, 31
	s_lshr_b32 s26, s1, 27
	s_add_i32 s26, s0, s26
	s_ashr_i32 s26, s26, 5
	s_mul_i32 s26, s26, 6
	s_ashr_i32 s27, s26, 31
	s_lshl_b64 s[26:27], s[26:27], 13
	v_lshl_add_u64 v[30:31], v[4:5], 0, s[26:27]
	s_waitcnt lgkmcnt(0)
	s_barrier
	global_load_dwordx4 v[26:29], v[6:7], off
	s_nop 0
	global_load_dwordx4 v[30:33], v[30:31], off
	v_lshl_add_u64 v[34:35], v[10:11], 0, s[26:27]
	v_lshl_add_u64 v[38:39], v[12:13], 0, s[26:27]
	global_load_dwordx4 v[34:37], v[34:35], off
	s_nop 0
	global_load_dwordx4 v[38:41], v[38:39], off
	s_lshl_b64 s[30:31], s[0:1], 6
	s_add_u32 s1, s30, s40
	s_addc_u32 s35, s31, 0
	s_and_b32 s26, s0, 7
	s_or_b32 s34, s1, s26
	s_lshl_b64 s[26:27], s[34:35], 12
	s_mov_b32 s57, 0
	global_load_dwordx4 v[188:191], v[8:9], off
	v_lshl_add_u64 v[184:185], v[16:17], 0, s[26:27]
	v_lshl_add_u64 v[186:187], v[14:15], 0, s[26:27]
	global_load_dwordx2 v[88:89], v[184:185], off nt
	global_load_dwordx2 v[84:85], v[184:185], off offset:512 nt
	global_load_dwordx2 v[82:83], v[184:185], off offset:1024 nt
	global_load_dwordx2 v[80:81], v[184:185], off offset:1536 nt
	global_load_dwordx2 v[78:79], v[184:185], off offset:2048 nt
	global_load_dwordx2 v[76:77], v[184:185], off offset:2560 nt
	global_load_dwordx2 v[70:71], v[184:185], off offset:3072 nt
	global_load_dwordx2 v[68:69], v[184:185], off offset:3584 nt
	global_load_dwordx2 v[86:87], v[186:187], off nt
	global_load_dwordx2 v[74:75], v[186:187], off offset:512 nt
	global_load_dwordx2 v[72:73], v[186:187], off offset:1024 nt
	global_load_dwordx2 v[66:67], v[186:187], off offset:1536 nt
	global_load_dwordx2 v[64:65], v[186:187], off offset:2048 nt
	global_load_dwordx2 v[58:59], v[186:187], off offset:2560 nt
	global_load_dwordx2 v[60:61], v[186:187], off offset:3072 nt
	global_load_dwordx2 v[62:63], v[186:187], off offset:3584 nt
	s_waitcnt vmcnt(21)
	ds_write2st64_b32 v178, v146, v147 offset0:0 offset1:32
	ds_write2st64_b32 v178, v148, v149 offset0:64 offset1:96
	ds_write2st64_b32 v178, v150, v151 offset0:128 offset1:160
	ds_write2st64_b32 v178, v152, v153 offset0:192 offset1:224
	ds_write2st64_b32 v178, v154, v155 offset0:8 offset1:40
	ds_write2st64_b32 v178, v156, v157 offset0:72 offset1:104
	ds_write2st64_b32 v178, v158, v159 offset0:136 offset1:168
	ds_write2st64_b32 v178, v160, v161 offset0:200 offset1:232
	ds_write2st64_b32 v178, v162, v163 offset0:16 offset1:48
	ds_write2st64_b32 v178, v164, v165 offset0:80 offset1:112
	ds_write2st64_b32 v178, v166, v167 offset0:144 offset1:176
	ds_write2st64_b32 v178, v168, v169 offset0:208 offset1:240
	ds_write2st64_b32 v178, v170, v171 offset0:24 offset1:56
	ds_write2st64_b32 v178, v172, v173 offset0:88 offset1:120
	ds_write2st64_b32 v178, v174, v175 offset0:152 offset1:184
	ds_write2st64_b32 v178, v176, v177 offset0:216 offset1:248
	s_waitcnt vmcnt(17) lgkmcnt(0)
	v_pk_mul_f32 v[28:29], v[32:33], v[28:29]
	v_pk_mul_f32 v[26:27], v[30:31], v[26:27]
	ds_write_b128 v100, v[26:29]
	v_pk_add_f32 v[36:37], v[36:37], 1.0 op_sel_hi:[1,0]
	v_pk_add_f32 v[34:35], v[34:35], 1.0 op_sel_hi:[1,0]
	ds_write_b128 v102, v[38:41]
	s_waitcnt vmcnt(16) lgkmcnt(0)
	v_pk_mul_f32 v[28:29], v[190:191], v[36:37]
	v_pk_mul_f32 v[26:27], v[188:189], v[34:35]
	ds_write_b128 v101, v[26:29]
	s_waitcnt lgkmcnt(0)
	s_barrier
	s_waitcnt vmcnt(15)
	v_mov_b64_e32 v[28:29], v[88:89]
	s_waitcnt vmcnt(14)
	v_mov_b64_e32 v[32:33], v[84:85]
	s_waitcnt vmcnt(13)
	v_mov_b64_e32 v[36:37], v[82:83]
	s_waitcnt vmcnt(12)
	v_mov_b64_e32 v[40:41], v[80:81]
	s_waitcnt vmcnt(11)
	v_mov_b64_e32 v[44:45], v[78:79]
	s_waitcnt vmcnt(10)
	v_mov_b64_e32 v[48:49], v[76:77]
	s_waitcnt vmcnt(9)
	v_mov_b64_e32 v[52:53], v[70:71]
	s_waitcnt vmcnt(8)
	v_mov_b64_e32 v[56:57], v[68:69]
	s_waitcnt vmcnt(7)
	v_mov_b64_e32 v[26:27], v[86:87]
	s_waitcnt vmcnt(6)
	v_mov_b64_e32 v[30:31], v[74:75]
	s_waitcnt vmcnt(5)
	v_mov_b64_e32 v[34:35], v[72:73]
	s_waitcnt vmcnt(4)
	v_mov_b64_e32 v[38:39], v[66:67]
	s_waitcnt vmcnt(3)
	v_mov_b64_e32 v[42:43], v[64:65]
	s_waitcnt vmcnt(2)
	v_mov_b64_e32 v[46:47], v[58:59]
	s_waitcnt vmcnt(1)
	v_mov_b64_e32 v[50:51], v[60:61]
	s_waitcnt vmcnt(0)
	v_mov_b64_e32 v[54:55], v[62:63]
	s_branch .LBB0_1307

; template <int YMODE, int EXTRA, bool NORM_OUT, bool XN8  , bool XIN_BF = false  , bool XOUT_BF = false  > ...
;     ...
;     if (EXTRA) {
;         for (int k = F.tid; k < D; k += NTHR) { const f32x4 a = *(const f32x4*)(wex + (size_t)k * ldw), b = *(const f32x4*)(wex + (size_t)k * ldw + 4);
;             we[0 * D + k] = a[0]; we[1 * D + k] = a[1]; we[2 * D + k] = a[2]; we[3 * D + k] = a[3]; we[4 * D + k] = b[0]; we[5 * D + k] = b[1]; we[6 * D + k] = b[2]; we[7 * D + k] = b[3]; }
;     }
;     if (YMODE == 2) { if (F.tid == 0) { int cum = 0; for (int e = 0; e < NE; ++e) { cumt[e] = cum; cum += (int)((__hip_atomic_load(cntw + e, __ATOMIC_RELAXED, __HIP_MEMORY_SCOPE_AGENT) + 255u) >> 8); } } }
;     for (int blk = blockIdx.x; blk < M / 64; blk += F.G) {
.LBB0_2171:
	v_lshl_add_u64 v[16:17], v[2:3], 0, s[10:11]
	v_lshl_add_u64 v[18:19], v[16:17], 0, s[10:11]
	v_lshl_add_u64 v[20:21], v[18:19], 0, s[10:11]
	global_load_dwordx4 v[142:145], v[2:3], off
	global_load_dwordx4 v[146:149], v[2:3], off offset:16
	global_load_dwordx4 v[150:153], v[16:17], off
	global_load_dwordx4 v[156:159], v[16:17], off offset:16
	global_load_dwordx4 v[160:163], v[18:19], off
	global_load_dwordx4 v[164:167], v[18:19], off offset:16
	global_load_dwordx4 v[168:171], v[20:21], off
	global_load_dwordx4 v[178:181], v[20:21], off offset:16
	v_mov_b32_e32 v182, v5
	s_cmpk_gt_i32 s2, 0xff
	s_cbranch_scc1 .LBB0_2197
	s_add_u32 s3, s50, 0x400000
	v_lshlrev_b32_e32 v2, 2, v1
	v_mov_b32_e32 v3, 0
	v_writelane_b32 v255, s12, 40
	s_addc_u32 s4, s51, 0
	v_lshl_add_u64 v[12:13], s[50:51], 0, v[2:3]
	v_lshl_add_u64 v[8:9], s[0:1], 0, v[2:3]
	s_mov_b64 s[0:1], 0x168000
	v_writelane_b32 v255, s13, 41
	s_add_u32 s36, s50, 0x420000
	s_mov_b64 s[8:9], 0x164000
	v_lshl_add_u64 v[10:11], v[12:13], 0, s[0:1]
	s_mov_b64 s[0:1], 0x166000
	s_addc_u32 s37, s51, 0
	v_lshl_add_u64 v[4:5], v[12:13], 0, s[8:9]
	s_add_i32 s5, 0, 0x10000
	v_lshl_add_u64 v[12:13], v[12:13], 0, s[0:1]
	v_readlane_b32 s0, v255, 9
	v_lshlrev_b32_e32 v16, 3, v194
	v_mov_b32_e32 v17, v3
	v_add_u32_e32 v1, s5, v2
	s_lshl_b32 s5, s0, 3
	v_lshl_add_u64 v[14:15], s[50:51], 0, v[16:17]
	s_mov_b64 s[0:1], 0x32a00000
	v_lshl_add_u64 v[14:15], v[14:15], 0, s[0:1]
	s_add_i32 s0, 0, 0x16010
	v_writelane_b32 v255, s0, 15
	s_add_i32 s0, 0, 0x16020
	v_writelane_b32 v255, s0, 13
	s_add_i32 s0, 0, 0x16030
	v_writelane_b32 v255, s0, 21
	s_add_i32 s0, 0, 0x16040
	v_writelane_b32 v255, s0, 19
	s_add_i32 s0, 0, 0x16050
	v_writelane_b32 v255, s0, 20
	s_add_i32 s0, 0, 0x16060
	v_writelane_b32 v255, s0, 17
	s_add_i32 s0, 0, 0x16070
	v_writelane_b32 v255, s0, 33
	s_add_i32 s0, 0, 0x16080
	v_writelane_b32 v255, s0, 39
	s_add_i32 s0, 0, 0x16090
	v_writelane_b32 v255, s0, 10
	s_add_i32 s0, 0, 0x160a0
	v_writelane_b32 v255, s0, 25
	s_add_i32 s0, 0, 0x160b0
	v_writelane_b32 v255, s0, 27
	s_add_i32 s0, 0, 0x160c0
	v_writelane_b32 v255, s0, 32
	s_add_i32 s0, 0, 0x160d0
	v_writelane_b32 v255, s0, 35
	s_add_i32 s0, 0, 0x160e0
	v_writelane_b32 v255, s0, 37
	s_add_i32 s0, 0, 0x160f0
	v_writelane_b32 v255, s0, 28
	s_add_i32 s0, 0, 0x16100
	v_writelane_b32 v255, s0, 30
	s_add_i32 s0, 0, 0x16110
	v_writelane_b32 v255, s0, 14
	s_add_i32 s0, 0, 0x16120
	v_writelane_b32 v255, s0, 23
	s_add_i32 s0, 0, 0x16130
	v_writelane_b32 v255, s0, 42
	s_add_i32 s0, 0, 0x16140
	v_writelane_b32 v255, s0, 43
	s_add_i32 s0, 0, 0x16150
	v_writelane_b32 v255, s0, 44
	s_add_i32 s0, 0, 0x16160
	v_writelane_b32 v255, s0, 45
	s_add_i32 s0, 0, 0x16170
	v_writelane_b32 v255, s0, 46
	s_add_i32 s0, 0, 0x16180
	v_writelane_b32 v255, s0, 47
	s_add_i32 s0, 0, 0x16190
	v_writelane_b32 v255, s0, 48
	s_add_i32 s0, 0, 0x161a0
	v_writelane_b32 v255, s0, 49
	s_add_i32 s0, 0, 0x161b0
	v_lshl_add_u64 v[6:7], s[6:7], 0, v[2:3]
	s_mov_b64 s[6:7], 0x2000
	v_writelane_b32 v255, s0, 50
	s_add_i32 s0, 0, 0x161c0
	v_lshl_add_u64 v[6:7], v[6:7], 0, s[6:7]
	v_lshl_add_u64 v[8:9], v[8:9], 0, s[6:7]
	s_add_i32 s6, 0, 0x12000
	s_add_i32 s7, 0, 0x14000
	v_lshlrev_b32_e32 v18, 4, v194
	v_writelane_b32 v255, s0, 51
	s_add_i32 s0, 0, 0x161d0
	v_add_u32_e32 v114, s6, v2
	v_add_u32_e32 v115, s7, v2
	v_lshlrev_b32_e32 v2, 2, v194
	v_add_u32_e32 v116, s6, v18
	v_add_u32_e32 v117, s7, v18
	v_add_u32_e32 v118, 0, v18
	v_lshlrev_b32_e32 v18, 2, v0
	v_mov_b32_e32 v19, v3
	v_lshlrev_b32_e32 v20, 4, v0
	v_mov_b32_e32 v21, v3
	v_writelane_b32 v255, s0, 52
	s_add_i32 s0, 0, 0x161f0
	v_lshl_add_u64 v[16:17], s[72:73], 0, v[16:17]
	v_cmp_eq_u32_e64 s[6:7], 0, v194
	v_cmp_gt_u32_e64 s[8:9], 8, v0
	v_lshl_add_u64 v[18:19], s[50:51], 0, v[18:19]
	v_lshlrev_b32_e32 v119, 14, v0
	v_cmp_gt_u32_e64 s[10:11], 64, v0
	v_lshlrev_b32_e32 v120, 4, v0
	v_lshlrev_b32_e32 v121, 3, v0
	v_lshl_add_u64 v[20:21], s[28:29], 0, v[20:21]
	v_lshl_add_u64 v[22:23], s[60:61], 0, v[2:3]
	s_lshl_b32 s33, s2, 6
	s_lshl_b32 s44, s48, 6
	v_mov_b32_e32 v122, 0x358637bd
	s_mov_b32 s45, 0xf800000
	v_mov_b32_e32 v123, 0x260
	s_mov_b32 s46, 0xc2fe0000
	s_mov_b32 s47, 0x40c0c00
	s_add_i32 s83, 0, 0x161e0
	v_writelane_b32 v255, s0, 53
	s_add_i32 s88, 0, 0x16200
	s_add_i32 s89, 0, 0x16210
	s_add_i32 s90, 0, 0x16220
	s_add_i32 s91, 0, 0x16230
	s_add_i32 s92, 0, 0x16240
	s_add_i32 s93, 0, 0x16250
	s_add_i32 s94, 0, 0x16260
	s_add_i32 s95, 0, 0x16270
	s_add_i32 s96, 0, 0x16280
	s_add_i32 s97, 0, 0x16290
	s_add_i32 s34, 0, 0x162a0
	s_add_i32 s35, 0, 0x162b0
	s_add_i32 s49, 0, 0x162c0
	s_add_i32 s52, 0, 0x162d0
	s_add_i32 s53, 0, 0x162e0
	s_add_i32 s54, 0, 0x162f0
	s_add_i32 s55, 0, 0x16300
	s_add_i32 s56, 0, 0x16310
	s_add_i32 s57, 0, 0x16320
	s_add_i32 s62, 0, 0x16330
	s_add_i32 s63, 0, 0x16340
	s_add_i32 s64, 0, 0x16350
	s_add_i32 s65, 0, 0x16360
	s_add_i32 s66, 0, 0x16370
	s_add_i32 s67, 0, 0x16380
	s_add_i32 s68, 0, 0x16390
	s_add_i32 s69, 0, 0x163a0
	s_add_i32 s70, 0, 0x163b0
	s_add_i32 s71, 0, 0x163c0
	s_add_i32 s74, 0, 0x163d0
	s_add_i32 s75, 0, 0x163e0
	v_mov_b32_e32 v124, 0x3a000000
	v_mov_b32_e32 v125, 0x42fe0000
	v_mov_b32_e32 v126, 0xff61b1e6
	v_mov_b32_e32 v127, 0x7f800000
	s_add_i32 s76, 0, 0x163f0
	s_mov_b32 s38, s2
	s_branch .LBB0_2175

; #define LAS __attribute__((address_space(3)))
; template <int YMODE, int EXTRA, bool NORM_OUT, bool XN8  , bool XIN_BF = false  , bool XOUT_BF = false  > ...
;     ...
;         for (int k = F.tid; k < D; k += NTHR) { const f32x4 a = *(const f32x4*)(wex + (size_t)k * ldw), b = *(const f32x4*)(wex + (size_t)k * ldw + 4);
;             we[0 * D + k] = a[0]; we[1 * D + k] = a[1]; we[2 * D + k] = a[2]; we[3 * D + k] = a[3]; we[4 * D + k] = b[0]; we[5 * D + k] = b[1]; we[6 * D + k] = b[2]; we[7 * D + k] = b[3]; }
;     }
;     if (YMODE == 2) { if (F.tid == 0) { int cum = 0; for (int e = 0; e < NE; ++e) { cumt[e] = cum; cum += (int)((__hip_atomic_load(cntw + e, __ATOMIC_RELAXED, __HIP_MEMORY_SCOPE_AGENT) + 255u) >> 8); } } }
;     for (int blk = blockIdx.x; blk < M / 64; blk += F.G) {
;         const int b = (blk * 64) / SEQ;
;         __syncthreads();
;         { const int col = 4 * F.tid;
;             if (YMODE) { const f32x4 g = *(const f32x4*)(gt + (size_t)b * 6 * D + col), p = *(const f32x4*)(gpost + col); *(LAS f32x4*)(vA + col) = g * p; }
;             if (NORM_OUT) { const f32x4 g = *(const f32x4*)(gpre + col), s = *(const f32x4*)(sc + (size_t)b * 6 * D + col); *(LAS f32x4*)(vB + col) = g * (1.f + s); *(LAS f32x4*)(vC + col) = *(const f32x4*)(sh + (size_t)b * 6 * D + col); } }
;         __syncthreads();
;         f32x4 xr[8]; u32x2 xrb[8], yr[8], yr2[8]; float w1n = 0.f, w2n = 0.f;
;     ...
;         RP_LOAD(0);
.LBB0_2175:
	s_ashr_i32 s39, s38, 31
	s_lshr_b32 s0, s39, 27
	s_add_i32 s0, s38, s0
	s_ashr_i32 s0, s0, 5
	s_mul_i32 s0, s0, 6
	s_ashr_i32 s1, s0, 31
	s_lshl_b64 s[0:1], s[0:1], 13
	v_lshl_add_u64 v[28:29], v[4:5], 0, s[0:1]
	s_waitcnt lgkmcnt(0)
	s_barrier
	global_load_dwordx4 v[24:27], v[6:7], off
	s_nop 0
	global_load_dwordx4 v[28:31], v[28:29], off
	v_lshl_add_u64 v[32:33], v[10:11], 0, s[0:1]
	v_lshl_add_u64 v[36:37], v[12:13], 0, s[0:1]
	global_load_dwordx4 v[32:35], v[32:33], off
	s_nop 0
	global_load_dwordx4 v[36:39], v[36:37], off
	s_lshl_b64 s[40:41], s[38:39], 6
	s_add_u32 s39, s40, s5
	s_addc_u32 s43, s41, 0
	s_and_b32 s0, s38, 7
	s_or_b32 s42, s39, s0
	s_lshl_b64 s[0:1], s[42:43], 12
	s_mov_b32 s77, 0
	global_load_dwordx4 v[188:191], v[8:9], off
	v_lshl_add_u64 v[184:185], v[16:17], 0, s[0:1]
	v_lshl_add_u64 v[186:187], v[14:15], 0, s[0:1]
	global_load_dwordx2 v[96:97], v[184:185], off nt
	global_load_dwordx2 v[86:87], v[184:185], off offset:512 nt
	global_load_dwordx2 v[82:83], v[184:185], off offset:1024 nt
	global_load_dwordx2 v[80:81], v[184:185], off offset:1536 nt
	global_load_dwordx2 v[70:71], v[184:185], off offset:2048 nt
	global_load_dwordx2 v[68:69], v[184:185], off offset:2560 nt
	global_load_dwordx2 v[66:67], v[184:185], off offset:3072 nt
	global_load_dwordx2 v[64:65], v[184:185], off offset:3584 nt
	global_load_dwordx2 v[78:79], v[186:187], off nt
	global_load_dwordx2 v[76:77], v[186:187], off offset:512 nt
	global_load_dwordx2 v[74:75], v[186:187], off offset:1024 nt
	global_load_dwordx2 v[72:73], v[186:187], off offset:1536 nt
	global_load_dwordx2 v[62:63], v[186:187], off offset:2048 nt
	global_load_dwordx2 v[60:61], v[186:187], off offset:2560 nt
	global_load_dwordx2 v[56:57], v[186:187], off offset:3072 nt
	global_load_dwordx2 v[58:59], v[186:187], off offset:3584 nt
	s_waitcnt vmcnt(21)
	ds_write2st64_b32 v182, v142, v143 offset0:0 offset1:32
	ds_write2st64_b32 v182, v144, v145 offset0:64 offset1:96
	ds_write2st64_b32 v182, v146, v147 offset0:128 offset1:160
	ds_write2st64_b32 v182, v148, v149 offset0:192 offset1:224
	ds_write2st64_b32 v182, v150, v151 offset0:8 offset1:40
	ds_write2st64_b32 v182, v152, v153 offset0:72 offset1:104
	ds_write2st64_b32 v182, v156, v157 offset0:136 offset1:168
	ds_write2st64_b32 v182, v158, v159 offset0:200 offset1:232
	ds_write2st64_b32 v182, v160, v161 offset0:16 offset1:48
	ds_write2st64_b32 v182, v162, v163 offset0:80 offset1:112
	ds_write2st64_b32 v182, v164, v165 offset0:144 offset1:176
	ds_write2st64_b32 v182, v166, v167 offset0:208 offset1:240
	ds_write2st64_b32 v182, v168, v169 offset0:24 offset1:56
	ds_write2st64_b32 v182, v170, v171 offset0:88 offset1:120
	ds_write2st64_b32 v182, v178, v179 offset0:152 offset1:184
	ds_write2st64_b32 v182, v180, v181 offset0:216 offset1:248
	s_waitcnt vmcnt(17) lgkmcnt(0)
	v_pk_mul_f32 v[26:27], v[30:31], v[26:27]
	v_pk_mul_f32 v[24:25], v[28:29], v[24:25]
	ds_write_b128 v1, v[24:27]
	v_pk_add_f32 v[34:35], v[34:35], 1.0 op_sel_hi:[1,0]
	v_pk_add_f32 v[32:33], v[32:33], 1.0 op_sel_hi:[1,0]
	ds_write_b128 v115, v[36:39]
	s_waitcnt vmcnt(16) lgkmcnt(0)
	v_pk_mul_f32 v[26:27], v[190:191], v[34:35]
	v_pk_mul_f32 v[24:25], v[188:189], v[32:33]
	ds_write_b128 v114, v[24:27]
	s_waitcnt lgkmcnt(0)
	s_barrier
	s_waitcnt vmcnt(15)
	v_mov_b64_e32 v[26:27], v[96:97]
	s_waitcnt vmcnt(14)
	v_mov_b64_e32 v[30:31], v[86:87]
	s_waitcnt vmcnt(13)
	v_mov_b64_e32 v[34:35], v[82:83]
	s_waitcnt vmcnt(12)
	v_mov_b64_e32 v[38:39], v[80:81]
	s_waitcnt vmcnt(11)
	v_mov_b64_e32 v[42:43], v[70:71]
	s_waitcnt vmcnt(10)
	v_mov_b64_e32 v[46:47], v[68:69]
	s_waitcnt vmcnt(9)
	v_mov_b64_e32 v[50:51], v[66:67]
	s_waitcnt vmcnt(8)
	v_mov_b64_e32 v[54:55], v[64:65]
	s_waitcnt vmcnt(7)
	v_mov_b64_e32 v[24:25], v[78:79]
	s_waitcnt vmcnt(6)
	v_mov_b64_e32 v[28:29], v[76:77]
	s_waitcnt vmcnt(5)
	v_mov_b64_e32 v[32:33], v[74:75]
	s_waitcnt vmcnt(4)
	v_mov_b64_e32 v[36:37], v[72:73]
	s_waitcnt vmcnt(3)
	v_mov_b64_e32 v[40:41], v[62:63]
	s_waitcnt vmcnt(2)
	v_mov_b64_e32 v[44:45], v[60:61]
	s_waitcnt vmcnt(1)
	v_mov_b64_e32 v[48:49], v[56:57]
	s_waitcnt vmcnt(0)
	v_mov_b64_e32 v[52:53], v[58:59]
	s_branch .LBB0_2177
